# v56 + GQA fast path: per-lane half-row partial sums accumulated in the loop, lane exchange of the row sum once per unit instead of once per tile
# baseline (speedup 1.0000x reference)
.LBB0_873:
	v_exp_f32_e32 v101, v80
	v_exp_f32_e32 v103, v81
	v_exp_f32_e32 v111, v88
	v_exp_f32_e32 v89, v89
	v_exp_f32_e32 v105, v82
	v_exp_f32_e32 v113, v90
	v_exp_f32_e32 v83, v83
	v_exp_f32_e32 v91, v91
	v_exp_f32_e32 v107, v84
	v_exp_f32_e32 v115, v92
	v_mov_b32_e32 v100, v64
	v_mov_b32_e32 v102, v65
	v_mov_b32_e32 v110, v72
	v_mov_b32_e32 v88, v73
	v_exp_f32_e32 v85, v85
	v_exp_f32_e32 v93, v93
	v_pk_add_f32 v[80:81], v[100:101], v[102:103]
	v_pk_add_f32 v[118:119], v[110:111], v[88:89]
	v_mov_b32_e32 v104, v66
	v_mov_b32_e32 v112, v74
	v_exp_f32_e32 v109, v86
	v_exp_f32_e32 v117, v94
	v_pk_add_f32 v[80:81], v[104:105], v[80:81]
	v_pk_add_f32 v[118:119], v[112:113], v[118:119]
	v_mov_b32_e32 v82, v67
	v_mov_b32_e32 v90, v75
	v_exp_f32_e32 v87, v87
	v_exp_f32_e32 v95, v95
	v_pk_add_f32 v[80:81], v[82:83], v[80:81]
	v_pk_add_f32 v[118:119], v[90:91], v[118:119]
	v_mov_b32_e32 v106, v68
	v_mov_b32_e32 v114, v76
	v_pk_add_f32 v[80:81], v[106:107], v[80:81]
	v_pk_add_f32 v[118:119], v[114:115], v[118:119]
	v_mov_b32_e32 v84, v69
	v_mov_b32_e32 v92, v77
	v_pk_add_f32 v[80:81], v[84:85], v[80:81]
	v_pk_add_f32 v[118:119], v[92:93], v[118:119]
	v_mov_b32_e32 v108, v70
	v_mov_b32_e32 v116, v78
	v_pk_add_f32 v[80:81], v[108:109], v[80:81]
	v_pk_add_f32 v[118:119], v[116:117], v[118:119]
	v_mov_b32_e32 v86, v71
	v_mov_b32_e32 v94, v79
	v_pk_add_f32 v[80:81], v[86:87], v[80:81]
	v_pk_add_f32 v[118:119], v[94:95], v[118:119]
	s_lshl_b32 s2, s33, 12
	v_pk_add_f32 v[80:81], v[118:119], v[80:81]
	s_add_u32 s8, s35, s2
	v_pk_add_f32 v[80:81], v[80:81], v[80:81] op_sel:[0,1] op_sel_hi:[1,0]
	s_addc_u32 s9, s36, 0
	s_lshl_b32 s2, s28, 7
	v_add_f32_e32 v80, v80, v217
	v_mov_b32_e32 v99, v80
	s_ashr_i32 s3, s2, 31
	s_nop 0
	v_permlane32_swap_b32_e32 v80, v99
	s_lshl_b64 s[2:3], s[2:3], 1
	v_mov_b32_e32 v96, 0
	v_add_f32_e32 v98, v142, v143
	v_mov_b32_e32 v97, v80
	s_add_u32 s8, s8, s2
	v_pk_add_f32 v[80:81], v[96:97], v[98:99]
	v_cvt_pk_bf16_f32 v64, v64, v65
	v_cvt_pk_bf16_f32 v65, v66, v67
	v_cvt_pk_bf16_f32 v66, v68, v69
	v_cvt_pk_bf16_f32 v67, v70, v71
	v_cvt_pk_bf16_f32 v68, v72, v73
	v_cvt_pk_bf16_f32 v69, v74, v75
	v_cvt_pk_bf16_f32 v70, v76, v77
	v_cvt_pk_bf16_f32 v71, v78, v79
	v_cvt_pk_bf16_f32 v72, v101, v103
	v_cvt_pk_bf16_f32 v73, v105, v83
	v_cvt_pk_bf16_f32 v74, v107, v85
	v_cvt_pk_bf16_f32 v75, v109, v87
	v_cvt_pk_bf16_f32 v76, v111, v89
	v_cvt_pk_bf16_f32 v77, v113, v91
	v_cvt_pk_bf16_f32 v78, v115, v93
	v_cvt_pk_bf16_f32 v79, v117, v95
	s_addc_u32 s9, s9, s3
	v_fmac_f32_e32 v81, v80, v128
	ds_read_b64_tr_b16 v[82:83], v211 offset:0
	ds_read_b64_tr_b16 v[84:85], v211 offset:0x800
	ds_read_b64_tr_b16 v[86:87], v211 offset:0x1000
	ds_read_b64_tr_b16 v[88:89], v211 offset:0x1800
	ds_read_b64_tr_b16 v[90:91], v211 offset:0x2000
	ds_read_b64_tr_b16 v[92:93], v211 offset:0x2800
	ds_read_b64_tr_b16 v[94:95], v211 offset:0x3000
	ds_read_b64_tr_b16 v[96:97], v211 offset:0x3800
	s_waitcnt lgkmcnt(0)
	s_nop 0
	v_mfma_f32_32x32x16_bf16 v[0:15], v[82:85], v[64:67], v[0:15]
	ds_read_b64_tr_b16 v[82:83], v211 offset:0x200
	ds_read_b64_tr_b16 v[84:85], v211 offset:0xa00
	v_mfma_f32_32x32x16_bf16 v[0:15], v[86:89], v[68:71], v[0:15]
	ds_read_b64_tr_b16 v[86:87], v211 offset:0x1200
	ds_read_b64_tr_b16 v[88:89], v211 offset:0x1a00
	v_mfma_f32_32x32x16_bf16 v[0:15], v[90:93], v[72:75], v[0:15]
	ds_read_b64_tr_b16 v[90:91], v211 offset:0x2200
	ds_read_b64_tr_b16 v[92:93], v211 offset:0x2a00
	v_mfma_f32_32x32x16_bf16 v[0:15], v[94:97], v[76:79], v[0:15]
	ds_read_b64_tr_b16 v[94:95], v211 offset:0x3200
	ds_read_b64_tr_b16 v[96:97], v211 offset:0x3a00
	s_waitcnt lgkmcnt(0)
	v_mfma_f32_32x32x16_bf16 v[48:63], v[82:85], v[64:67], v[48:63]
	ds_read_b64_tr_b16 v[82:83], v211 offset:0x400
	ds_read_b64_tr_b16 v[84:85], v211 offset:0xc00
	v_mfma_f32_32x32x16_bf16 v[48:63], v[86:89], v[68:71], v[48:63]
	ds_read_b64_tr_b16 v[86:87], v211 offset:0x1400
	ds_read_b64_tr_b16 v[88:89], v211 offset:0x1c00
	v_mfma_f32_32x32x16_bf16 v[48:63], v[90:93], v[72:75], v[48:63]
	ds_read_b64_tr_b16 v[90:91], v211 offset:0x2400
	ds_read_b64_tr_b16 v[92:93], v211 offset:0x2c00
	v_mfma_f32_32x32x16_bf16 v[48:63], v[94:97], v[76:79], v[48:63]
	ds_read_b64_tr_b16 v[94:95], v211 offset:0x3400
	ds_read_b64_tr_b16 v[96:97], v211 offset:0x3c00
	s_waitcnt lgkmcnt(0)
	v_mfma_f32_32x32x16_bf16 v[32:47], v[82:85], v[64:67], v[32:47]
	ds_read_b64_tr_b16 v[82:83], v211 offset:0x600
	ds_read_b64_tr_b16 v[84:85], v211 offset:0xe00
	v_mfma_f32_32x32x16_bf16 v[32:47], v[86:89], v[68:71], v[32:47]
	ds_read_b64_tr_b16 v[86:87], v211 offset:0x1600
	ds_read_b64_tr_b16 v[88:89], v211 offset:0x1e00
	v_mfma_f32_32x32x16_bf16 v[32:47], v[90:93], v[72:75], v[32:47]
	ds_read_b64_tr_b16 v[90:91], v211 offset:0x2600
	ds_read_b64_tr_b16 v[92:93], v211 offset:0x2e00
	v_mfma_f32_32x32x16_bf16 v[32:47], v[94:97], v[76:79], v[32:47]
	ds_read_b64_tr_b16 v[94:95], v211 offset:0x3600
	ds_read_b64_tr_b16 v[96:97], v211 offset:0x3e00
	s_waitcnt lgkmcnt(0)
	v_mfma_f32_32x32x16_bf16 v[16:31], v[82:85], v[64:67], v[16:31]
	v_rcp_f32_e32 v67, v81
	v_mbcnt_lo_u32_b32 v66, -1, 0
	v_mbcnt_hi_u32_b32 v66, -1, v66
	s_add_i32 s20, s20, 1
	v_add_u32_e32 v64, s80, v66
	v_ashrrev_i32_e32 v64, 1, v64
	v_mul_f32_e32 v0, v67, v0
	v_mul_f32_e32 v1, v67, v1
	v_bfi_b32 v64, s84, v64, v66
	v_cvt_pk_bf16_f32 v0, v0, v1
	v_mul_f32_e32 v1, v67, v2
	v_mul_f32_e32 v2, v67, v3
	v_ashrrev_i32_e32 v65, 31, v64
	v_cvt_pk_bf16_f32 v1, v1, v2
	v_mul_f32_e32 v2, v67, v4
	v_mul_f32_e32 v3, v67, v5
	v_lshlrev_b64 v[64:65], 12, v[64:65]
	v_lshrrev_b32_e32 v66, 1, v66
	v_cvt_pk_bf16_f32 v2, v2, v3
	v_mul_f32_e32 v3, v67, v6
	v_lshl_add_u64 v[64:65], s[8:9], 0, v[64:65]
	v_and_b32_e32 v128, 16, v66
	v_mul_f32_e32 v4, v67, v7
	v_cvt_pk_bf16_f32 v3, v3, v4
	v_lshl_add_u64 v[64:65], v[64:65], 0, v[128:129]
	v_permlane32_swap_b32_e32 v0, v2
	v_permlane32_swap_b32_e32 v1, v3
	global_store_dwordx4 v[64:65], v[0:3], off
	v_mul_f32_e32 v4, v67, v15
	v_mfma_f32_32x32x16_bf16 v[16:31], v[86:89], v[68:71], v[16:31]
	v_mul_f32_e32 v0, v67, v8
	v_mul_f32_e32 v1, v67, v9
	v_cvt_pk_bf16_f32 v0, v0, v1
	v_mul_f32_e32 v1, v67, v10
	v_mul_f32_e32 v2, v67, v11
	v_cvt_pk_bf16_f32 v1, v1, v2
	v_mul_f32_e32 v2, v67, v12
	v_mul_f32_e32 v3, v67, v13
	v_cvt_pk_bf16_f32 v2, v2, v3
	v_mul_f32_e32 v3, v67, v14
	v_cvt_pk_bf16_f32 v3, v3, v4
	v_permlane32_swap_b32_e32 v0, v2
	s_nop 0
	v_permlane32_swap_b32_e32 v1, v3
	global_store_dwordx4 v[64:65], v[0:3], off offset:32
	v_mul_f32_e32 v4, v67, v55
	v_mfma_f32_32x32x16_bf16 v[16:31], v[90:93], v[72:75], v[16:31]
	v_mul_f32_e32 v0, v67, v48
	v_mul_f32_e32 v1, v67, v49
	v_cvt_pk_bf16_f32 v0, v0, v1
	v_mul_f32_e32 v1, v67, v50
	v_mul_f32_e32 v2, v67, v51
	v_cvt_pk_bf16_f32 v1, v1, v2
	v_mul_f32_e32 v2, v67, v52
	v_mul_f32_e32 v3, v67, v53
	v_cvt_pk_bf16_f32 v2, v2, v3
	v_mul_f32_e32 v3, v67, v54
	v_cvt_pk_bf16_f32 v3, v3, v4
	v_permlane32_swap_b32_e32 v0, v2
	s_nop 0
	v_permlane32_swap_b32_e32 v1, v3
	global_store_dwordx4 v[64:65], v[0:3], off offset:64
	v_mul_f32_e32 v4, v67, v63
	v_mfma_f32_32x32x16_bf16 v[16:31], v[94:97], v[76:79], v[16:31]
	v_mul_f32_e32 v0, v67, v56
	v_mul_f32_e32 v1, v67, v57
	v_cvt_pk_bf16_f32 v0, v0, v1
	v_mul_f32_e32 v1, v67, v58
	v_mul_f32_e32 v2, v67, v59
	v_cvt_pk_bf16_f32 v1, v1, v2
	v_mul_f32_e32 v2, v67, v60
	v_mul_f32_e32 v3, v67, v61
	v_cvt_pk_bf16_f32 v2, v2, v3
	v_mul_f32_e32 v3, v67, v62
	v_cvt_pk_bf16_f32 v3, v3, v4
	v_permlane32_swap_b32_e32 v0, v2
	s_nop 0
	v_permlane32_swap_b32_e32 v1, v3
	global_store_dwordx4 v[64:65], v[0:3], off offset:96
	v_mul_f32_e32 v4, v67, v39
	s_lshl_b32 s2, s20, 8
	v_mul_f32_e32 v0, v67, v32
	v_mul_f32_e32 v1, v67, v33
	v_cvt_pk_bf16_f32 v0, v0, v1
	v_mul_f32_e32 v1, v67, v34
	v_mul_f32_e32 v2, v67, v35
	v_cvt_pk_bf16_f32 v1, v1, v2
	v_mul_f32_e32 v2, v67, v36
	v_mul_f32_e32 v3, v67, v37
	v_cvt_pk_bf16_f32 v2, v2, v3
	v_mul_f32_e32 v3, v67, v38
	v_cvt_pk_bf16_f32 v3, v3, v4
	v_permlane32_swap_b32_e32 v0, v2
	s_nop 0
	v_permlane32_swap_b32_e32 v1, v3
	global_store_dwordx4 v[64:65], v[0:3], off offset:128
	v_mul_f32_e32 v4, v67, v47
	s_add_i32 s3, s2, s94
	v_mul_f32_e32 v0, v67, v40
	v_mul_f32_e32 v1, v67, v41
	v_cvt_pk_bf16_f32 v0, v0, v1
	v_mul_f32_e32 v1, v67, v42
	v_mul_f32_e32 v2, v67, v43
	v_cvt_pk_bf16_f32 v1, v1, v2
	v_mul_f32_e32 v2, v67, v44
	v_mul_f32_e32 v3, v67, v45
	v_cvt_pk_bf16_f32 v2, v2, v3
	v_mul_f32_e32 v3, v67, v46
	v_cvt_pk_bf16_f32 v3, v3, v4
	v_permlane32_swap_b32_e32 v0, v2
	s_nop 0
	v_permlane32_swap_b32_e32 v1, v3
	global_store_dwordx4 v[64:65], v[0:3], off offset:160
	v_mul_f32_e32 v4, v67, v23
	s_cmp_lt_i32 s3, s37
	v_mul_f32_e32 v0, v67, v16
	v_mul_f32_e32 v1, v67, v17
	v_cvt_pk_bf16_f32 v0, v0, v1
	v_mul_f32_e32 v1, v67, v18
	v_mul_f32_e32 v2, v67, v19
	v_cvt_pk_bf16_f32 v1, v1, v2
	v_mul_f32_e32 v2, v67, v20
	v_mul_f32_e32 v3, v67, v21
	v_cvt_pk_bf16_f32 v2, v2, v3
	v_mul_f32_e32 v3, v67, v22
	v_cvt_pk_bf16_f32 v3, v3, v4
	v_permlane32_swap_b32_e32 v0, v2
	s_nop 0
	v_permlane32_swap_b32_e32 v1, v3
	global_store_dwordx4 v[64:65], v[0:3], off offset:192
	v_mul_f32_e32 v4, v67, v31
	s_movk_i32 s33, 0xffef
	v_mul_f32_e32 v0, v67, v24
	v_mul_f32_e32 v1, v67, v25
	v_cvt_pk_bf16_f32 v0, v0, v1
	v_mul_f32_e32 v1, v67, v26
	v_mul_f32_e32 v2, v67, v27
	v_cvt_pk_bf16_f32 v1, v1, v2
	v_mul_f32_e32 v2, v67, v28
	v_mul_f32_e32 v3, v67, v29
	v_cvt_pk_bf16_f32 v2, v2, v3
	v_mul_f32_e32 v3, v67, v30
	v_cvt_pk_bf16_f32 v3, v3, v4
	v_permlane32_swap_b32_e32 v0, v2
	s_nop 0
	v_permlane32_swap_b32_e32 v1, v3
	global_store_dwordx4 v[64:65], v[0:3], off offset:224
	s_cbranch_scc0 .LBB0_889

.LBB0_881:
	ds_read_b128 v[96:99], v216 offset:49152
	ds_read_b128 v[100:103], v216 offset:57344
	ds_read_b128 v[178:181], v218 offset:49152
	ds_read_b128 v[182:185], v218 offset:57344
	ds_read_b128 v[240:243], v219 offset:49152
	ds_read_b128 v[244:247], v219 offset:57344
	v_add_f32_e32 v88, v64, v65
	v_add_f32_e32 v89, v72, v73
	v_add_f32_e32 v90, v80, v81
	v_add_f32_e32 v91, v194, v195
	v_add_f32_e32 v88, v66, v88
	v_add_f32_e32 v89, v74, v89
	v_add_f32_e32 v90, v82, v90
	s_waitcnt lgkmcnt(4)
	v_mfma_f32_32x32x16_bf16 v[112:127], v[96:99], v[138:141], 0
	v_mfma_f32_32x32x16_bf16 v[96:111], v[100:103], v[138:141], 0
	v_add_f32_e32 v91, v196, v91
	v_add_f32_e32 v88, v67, v88
	v_add_f32_e32 v89, v75, v89
	v_add_f32_e32 v90, v83, v90
	v_add_f32_e32 v91, v197, v91
	v_add_f32_e32 v88, v68, v88
	v_add_f32_e32 v89, v76, v89
	s_waitcnt lgkmcnt(2)
	v_mfma_f32_32x32x16_bf16 v[112:127], v[178:181], v[154:157], v[112:127]
	v_mfma_f32_32x32x16_bf16 v[96:111], v[182:185], v[154:157], v[96:111]
	ds_read_b128 v[178:181], v220 offset:49152
	ds_read_b128 v[182:185], v220 offset:57344
	v_add_f32_e32 v90, v84, v90
	v_add_f32_e32 v91, v92, v91
	v_add_f32_e32 v88, v69, v88
	v_add_f32_e32 v89, v77, v89
	v_add_f32_e32 v90, v85, v90
	v_add_f32_e32 v91, v93, v91
	v_add_f32_e32 v88, v70, v88
	s_waitcnt lgkmcnt(2)
	v_mfma_f32_32x32x16_bf16 v[112:127], v[240:243], v[158:161], v[112:127]
	v_mfma_f32_32x32x16_bf16 v[96:111], v[244:247], v[158:161], v[96:111]
	ds_read_b128 v[240:243], v221 offset:49152
	ds_read_b128 v[244:247], v221 offset:57344
	v_add_f32_e32 v89, v78, v89
	v_add_f32_e32 v90, v86, v90
	v_add_f32_e32 v91, v94, v91
	v_add_f32_e32 v88, v71, v88
	v_add_f32_e32 v89, v79, v89
	v_add_f32_e32 v90, v87, v90
	v_add_f32_e32 v91, v95, v91
	s_waitcnt lgkmcnt(2)
	v_mfma_f32_32x32x16_bf16 v[112:127], v[178:181], v[150:153], v[112:127]
	v_mfma_f32_32x32x16_bf16 v[96:111], v[182:185], v[150:153], v[96:111]
	ds_read_b128 v[178:181], v222 offset:49152
	ds_read_b128 v[182:185], v222 offset:57344
	v_add_f32_e32 v88, v89, v88
	v_add_f32_e32 v89, v91, v90
	v_add_f32_e32 v227, v88, v89
	v_cvt_pk_bf16_f32 v88, v64, v65
	v_cvt_pk_bf16_f32 v89, v66, v67
	v_cvt_pk_bf16_f32 v90, v68, v69
	v_cvt_pk_bf16_f32 v91, v70, v71
	s_waitcnt lgkmcnt(2)
	v_mfma_f32_32x32x16_bf16 v[112:127], v[240:243], v[146:149], v[112:127]
	v_mfma_f32_32x32x16_bf16 v[96:111], v[244:247], v[146:149], v[96:111]
	ds_read_b128 v[240:243], v224 offset:49152
	ds_read_b128 v[244:247], v224 offset:57344
	v_cvt_pk_bf16_f32 v72, v72, v73
	v_cvt_pk_bf16_f32 v73, v74, v75
	v_cvt_pk_bf16_f32 v74, v76, v77
	v_cvt_pk_bf16_f32 v75, v78, v79
	s_waitcnt lgkmcnt(2)
	v_mfma_f32_32x32x16_bf16 v[112:127], v[178:181], v[142:145], v[112:127]
	v_mfma_f32_32x32x16_bf16 v[96:111], v[182:185], v[142:145], v[96:111]
	ds_read_b128 v[178:181], v223 offset:49152
	ds_read_b128 v[182:185], v223 offset:57344
	v_cvt_pk_bf16_f32 v64, v80, v81
	v_cvt_pk_bf16_f32 v65, v82, v83
	v_cvt_pk_bf16_f32 v66, v84, v85
	v_cvt_pk_bf16_f32 v67, v86, v87
	v_cvt_pk_bf16_f32 v68, v194, v195
	v_cvt_pk_bf16_f32 v69, v196, v197
	v_cvt_pk_bf16_f32 v70, v92, v93
	s_waitcnt lgkmcnt(2)
	v_mfma_f32_32x32x16_bf16 v[112:127], v[240:243], v[134:137], v[112:127]
	v_mfma_f32_32x32x16_bf16 v[96:111], v[244:247], v[134:137], v[96:111]
	v_cvt_pk_bf16_f32 v71, v94, v95
	s_waitcnt lgkmcnt(0)
	v_mfma_f32_32x32x16_bf16 v[112:127], v[178:181], v[130:133], v[112:127]
	v_mfma_f32_32x32x16_bf16 v[96:111], v[182:185], v[130:133], v[96:111]
	s_add_i32 s2, s39, -1
	s_mul_i32 s2, s2, s62
	s_lshl_b32 s72, s2, 6
	s_lshl_b64 s[2:3], s[72:73], 1
	s_add_u32 s12, s10, s2
	s_addc_u32 s13, s11, s3
	s_add_u32 s2, s8, s2
	s_addc_u32 s3, s9, s3
	global_load_dwordx4 v[178:181], v128, s[12:13]
	global_load_dwordx4 v[182:185], v198, s[12:13]
	global_load_dwordx4 v[186:189], v128, s[2:3]
	global_load_dwordx4 v[190:193], v198, s[2:3]
	ds_read_b64_tr_b16 v[76:77], v209 offset:0
	ds_read_b64_tr_b16 v[78:79], v209 offset:0x800
	ds_read_b64_tr_b16 v[80:81], v209 offset:0x1000
	ds_read_b64_tr_b16 v[82:83], v209 offset:0x1800
	ds_read_b64_tr_b16 v[84:85], v209 offset:0x2000
	ds_read_b64_tr_b16 v[86:87], v209 offset:0x2800
	ds_read_b64_tr_b16 v[92:93], v209 offset:0x3000
	ds_read_b64_tr_b16 v[94:95], v209 offset:0x3800
	s_waitcnt lgkmcnt(0)
	s_nop 0
	v_mfma_f32_32x32x16_bf16 v[0:15], v[76:79], v[88:91], v[0:15]
	v_mfma_f32_32x32x16_bf16 v[0:15], v[80:83], v[72:75], v[0:15]
	v_mfma_f32_32x32x16_bf16 v[0:15], v[84:87], v[64:67], v[0:15]
	ds_read_b64_tr_b16 v[76:77], v209 offset:0x200
	ds_read_b64_tr_b16 v[78:79], v209 offset:0xa00
	ds_read_b64_tr_b16 v[80:81], v209 offset:0x1200
	v_mfma_f32_32x32x16_bf16 v[0:15], v[92:95], v[68:71], v[0:15]
	ds_read_b64_tr_b16 v[82:83], v209 offset:0x1a00
	ds_read_b64_tr_b16 v[84:85], v209 offset:0x2200
	ds_read_b64_tr_b16 v[86:87], v209 offset:0x2a00
	ds_read_b64_tr_b16 v[92:93], v209 offset:0x3200
	ds_read_b64_tr_b16 v[94:95], v209 offset:0x3a00
	s_waitcnt lgkmcnt(0)
	v_mfma_f32_32x32x16_bf16 v[48:63], v[76:79], v[88:91], v[48:63]
	v_mfma_f32_32x32x16_bf16 v[48:63], v[80:83], v[72:75], v[48:63]
	v_mfma_f32_32x32x16_bf16 v[48:63], v[84:87], v[64:67], v[48:63]
	ds_read_b64_tr_b16 v[76:77], v209 offset:0x400
	ds_read_b64_tr_b16 v[78:79], v209 offset:0xc00
	ds_read_b64_tr_b16 v[80:81], v209 offset:0x1400
	ds_read_b64_tr_b16 v[82:83], v209 offset:0x1c00
	v_mfma_f32_32x32x16_bf16 v[48:63], v[92:95], v[68:71], v[48:63]
	ds_read_b64_tr_b16 v[84:85], v209 offset:0x2400
	ds_read_b64_tr_b16 v[86:87], v209 offset:0x2c00
	ds_read_b64_tr_b16 v[92:93], v209 offset:0x3400
	ds_read_b64_tr_b16 v[94:95], v209 offset:0x3c00
	s_waitcnt lgkmcnt(0)
	v_mfma_f32_32x32x16_bf16 v[32:47], v[76:79], v[88:91], v[32:47]
	ds_read_b64_tr_b16 v[76:77], v209 offset:0x600
	ds_read_b64_tr_b16 v[78:79], v209 offset:0xe00
	v_exp_f32_e32 v234, v104
	v_exp_f32_e32 v235, v105
	v_exp_f32_e32 v236, v106
	v_exp_f32_e32 v237, v107
	v_exp_f32_e32 v238, v108
	v_exp_f32_e32 v239, v109
	v_exp_f32_e32 v231, v110
	v_exp_f32_e32 v249, v111
	v_mfma_f32_32x32x16_bf16 v[32:47], v[80:83], v[72:75], v[32:47]
	v_exp_f32_e32 v80, v112
	v_exp_f32_e32 v81, v113
	v_exp_f32_e32 v82, v114
	v_exp_f32_e32 v83, v115
	v_mfma_f32_32x32x16_bf16 v[32:47], v[84:87], v[64:67], v[32:47]
	v_exp_f32_e32 v84, v116
	v_exp_f32_e32 v85, v117
	v_exp_f32_e32 v86, v118
	v_exp_f32_e32 v87, v119
	v_exp_f32_e32 v112, v96
	v_exp_f32_e32 v113, v97
	v_exp_f32_e32 v114, v98
	v_exp_f32_e32 v115, v99
	v_exp_f32_e32 v116, v100
	v_exp_f32_e32 v117, v101
	v_exp_f32_e32 v118, v102
	v_exp_f32_e32 v119, v103
	v_mfma_f32_32x32x16_bf16 v[32:47], v[92:95], v[68:71], v[32:47]
	ds_read_b64_tr_b16 v[92:93], v209 offset:0x1600
	ds_read_b64_tr_b16 v[94:95], v209 offset:0x1e00
	ds_read_b64_tr_b16 v[96:97], v209 offset:0x2600
	ds_read_b64_tr_b16 v[98:99], v209 offset:0x2e00
	ds_read_b64_tr_b16 v[100:101], v209 offset:0x3600
	ds_read_b64_tr_b16 v[102:103], v209 offset:0x3e00
	s_waitcnt lgkmcnt(0)
	v_mfma_f32_32x32x16_bf16 v[16:31], v[76:79], v[88:91], v[16:31]
	v_exp_f32_e32 v88, v120
	v_exp_f32_e32 v89, v121
	v_exp_f32_e32 v90, v122
	v_exp_f32_e32 v91, v123
	v_mfma_f32_32x32x16_bf16 v[16:31], v[92:95], v[72:75], v[16:31]
	v_exp_f32_e32 v92, v124
	v_exp_f32_e32 v93, v125
	v_exp_f32_e32 v94, v126
	v_exp_f32_e32 v95, v127
	s_barrier
	v_mfma_f32_32x32x16_bf16 v[16:31], v[96:99], v[64:67], v[16:31]
	s_waitcnt vmcnt(4)
	s_waitcnt vmcnt(7)
	ds_write_b128 v212, v[162:165]
	s_waitcnt vmcnt(6)
	ds_write_b128 v213, v[166:169]
	s_waitcnt vmcnt(5)
	ds_write_b128 v214, v[170:173] offset:32768
	s_waitcnt vmcnt(4)
	ds_write_b128 v215, v[174:177] offset:32768
	v_mfma_f32_32x32x16_bf16 v[16:31], v[100:103], v[68:71], v[16:31]
.LBB0_883:
	s_waitcnt lgkmcnt(0)
	s_barrier
	ds_read_b128 v[64:67], v216 offset:32768
	ds_read_b128 v[68:71], v216 offset:40960
	ds_read_b128 v[162:165], v218 offset:32768
	ds_read_b128 v[166:169], v218 offset:40960
	ds_read_b128 v[240:243], v219 offset:32768
	ds_read_b128 v[244:247], v219 offset:40960
	v_add_f32_e32 v120, v80, v81
	v_add_f32_e32 v121, v88, v89
	v_add_f32_e32 v122, v112, v113
	v_add_f32_e32 v123, v234, v235
	v_add_f32_e32 v120, v82, v120
	v_add_f32_e32 v121, v90, v121
	v_add_f32_e32 v122, v114, v122
	s_waitcnt lgkmcnt(4)
	v_mfma_f32_32x32x16_bf16 v[96:111], v[64:67], v[138:141], 0
	v_mfma_f32_32x32x16_bf16 v[64:79], v[68:71], v[138:141], 0
	v_add_f32_e32 v123, v236, v123
	v_add_f32_e32 v120, v83, v120
	v_add_f32_e32 v121, v91, v121
	v_add_f32_e32 v122, v115, v122
	v_add_f32_e32 v123, v237, v123
	v_add_f32_e32 v120, v84, v120
	v_add_f32_e32 v121, v92, v121
	s_waitcnt lgkmcnt(2)
	v_mfma_f32_32x32x16_bf16 v[96:111], v[162:165], v[154:157], v[96:111]
	v_mfma_f32_32x32x16_bf16 v[64:79], v[166:169], v[154:157], v[64:79]
	ds_read_b128 v[162:165], v220 offset:32768
	ds_read_b128 v[166:169], v220 offset:40960
	v_add_f32_e32 v122, v116, v122
	v_add_f32_e32 v123, v238, v123
	v_add_f32_e32 v120, v85, v120
	v_add_f32_e32 v121, v93, v121
	v_add_f32_e32 v122, v117, v122
	v_add_f32_e32 v123, v239, v123
	v_add_f32_e32 v120, v86, v120
	s_waitcnt lgkmcnt(2)
	v_mfma_f32_32x32x16_bf16 v[96:111], v[240:243], v[158:161], v[96:111]
	v_mfma_f32_32x32x16_bf16 v[64:79], v[244:247], v[158:161], v[64:79]
	ds_read_b128 v[240:243], v221 offset:32768
	ds_read_b128 v[244:247], v221 offset:40960
	v_add_f32_e32 v121, v94, v121
	v_add_f32_e32 v122, v118, v122
	v_add_f32_e32 v123, v231, v123
	v_add_f32_e32 v120, v87, v120
	v_add_f32_e32 v121, v95, v121
	v_add_f32_e32 v122, v119, v122
	v_add_f32_e32 v123, v249, v123
	s_waitcnt lgkmcnt(2)
	v_mfma_f32_32x32x16_bf16 v[96:111], v[162:165], v[150:153], v[96:111]
	v_mfma_f32_32x32x16_bf16 v[64:79], v[166:169], v[150:153], v[64:79]
	ds_read_b128 v[162:165], v222 offset:32768
	ds_read_b128 v[166:169], v222 offset:40960
	v_add_f32_e32 v120, v121, v120
	v_add_f32_e32 v121, v123, v122
	v_add_f32_e32 v229, v120, v121
	v_cvt_pk_bf16_f32 v124, v80, v81
	v_cvt_pk_bf16_f32 v125, v82, v83
	v_cvt_pk_bf16_f32 v126, v84, v85
	s_waitcnt lgkmcnt(2)
	v_mfma_f32_32x32x16_bf16 v[96:111], v[240:243], v[146:149], v[96:111]
	v_mfma_f32_32x32x16_bf16 v[64:79], v[244:247], v[146:149], v[64:79]
	ds_read_b128 v[240:243], v224 offset:32768
	ds_read_b128 v[244:247], v224 offset:40960
	v_cvt_pk_bf16_f32 v127, v86, v87
	v_cvt_pk_bf16_f32 v120, v88, v89
	v_cvt_pk_bf16_f32 v121, v90, v91
	v_cvt_pk_bf16_f32 v122, v92, v93
	v_cvt_pk_bf16_f32 v123, v94, v95
	v_cvt_pk_bf16_f32 v112, v112, v113
	v_cvt_pk_bf16_f32 v113, v114, v115
	s_waitcnt lgkmcnt(2)
	v_mfma_f32_32x32x16_bf16 v[96:111], v[162:165], v[142:145], v[96:111]
	v_mfma_f32_32x32x16_bf16 v[64:79], v[166:169], v[142:145], v[64:79]
	ds_read_b128 v[162:165], v223 offset:32768
	ds_read_b128 v[166:169], v223 offset:40960
	v_cvt_pk_bf16_f32 v114, v116, v117
	v_cvt_pk_bf16_f32 v115, v118, v119
	v_cvt_pk_bf16_f32 v116, v234, v235
	v_cvt_pk_bf16_f32 v117, v236, v237
	v_cvt_pk_bf16_f32 v118, v238, v239
	v_cvt_pk_bf16_f32 v119, v231, v249
	s_waitcnt lgkmcnt(2)
	v_mfma_f32_32x32x16_bf16 v[96:111], v[240:243], v[134:137], v[96:111]
	v_mfma_f32_32x32x16_bf16 v[64:79], v[244:247], v[134:137], v[64:79]
	s_waitcnt lgkmcnt(0)
	v_mfma_f32_32x32x16_bf16 v[96:111], v[162:165], v[130:133], v[96:111]
	v_mfma_f32_32x32x16_bf16 v[64:79], v[166:169], v[130:133], v[64:79]
	s_min_i32 s2, s39, s14
	s_mul_i32 s2, s2, s62
	s_lshl_b32 s72, s2, 6
	s_lshl_b64 s[2:3], s[72:73], 1
	s_add_u32 s12, s10, s2
	s_addc_u32 s13, s11, s3
	s_add_u32 s2, s8, s2
	s_addc_u32 s3, s9, s3
	global_load_dwordx4 v[162:165], v128, s[12:13]
	global_load_dwordx4 v[166:169], v198, s[12:13]
	global_load_dwordx4 v[170:173], v128, s[2:3]
	global_load_dwordx4 v[174:177], v198, s[2:3]
	ds_read_b64_tr_b16 v[80:81], v211 offset:0
	ds_read_b64_tr_b16 v[82:83], v211 offset:0x800
	ds_read_b64_tr_b16 v[84:85], v211 offset:0x1000
	ds_read_b64_tr_b16 v[86:87], v211 offset:0x1800
	ds_read_b64_tr_b16 v[88:89], v211 offset:0x2000
	ds_read_b64_tr_b16 v[90:91], v211 offset:0x2800
	ds_read_b64_tr_b16 v[92:93], v211 offset:0x3000
	ds_read_b64_tr_b16 v[94:95], v211 offset:0x3800
	s_waitcnt lgkmcnt(0)
	s_nop 0
	v_mfma_f32_32x32x16_bf16 v[0:15], v[80:83], v[124:127], v[0:15]
	v_mfma_f32_32x32x16_bf16 v[0:15], v[84:87], v[120:123], v[0:15]
	v_mfma_f32_32x32x16_bf16 v[0:15], v[88:91], v[112:115], v[0:15]
	ds_read_b64_tr_b16 v[80:81], v211 offset:0x200
	ds_read_b64_tr_b16 v[82:83], v211 offset:0xa00
	ds_read_b64_tr_b16 v[84:85], v211 offset:0x1200
	v_mfma_f32_32x32x16_bf16 v[0:15], v[92:95], v[116:119], v[0:15]
	ds_read_b64_tr_b16 v[86:87], v211 offset:0x1a00
	ds_read_b64_tr_b16 v[88:89], v211 offset:0x2200
	ds_read_b64_tr_b16 v[90:91], v211 offset:0x2a00
	ds_read_b64_tr_b16 v[92:93], v211 offset:0x3200
	ds_read_b64_tr_b16 v[94:95], v211 offset:0x3a00
	s_waitcnt lgkmcnt(0)
	v_mfma_f32_32x32x16_bf16 v[48:63], v[80:83], v[124:127], v[48:63]
	v_mfma_f32_32x32x16_bf16 v[48:63], v[84:87], v[120:123], v[48:63]
	v_mfma_f32_32x32x16_bf16 v[48:63], v[88:91], v[112:115], v[48:63]
	ds_read_b64_tr_b16 v[80:81], v211 offset:0x400
	ds_read_b64_tr_b16 v[82:83], v211 offset:0xc00
	ds_read_b64_tr_b16 v[84:85], v211 offset:0x1400
	ds_read_b64_tr_b16 v[86:87], v211 offset:0x1c00
	v_mfma_f32_32x32x16_bf16 v[48:63], v[92:95], v[116:119], v[48:63]
	ds_read_b64_tr_b16 v[88:89], v211 offset:0x2400
	ds_read_b64_tr_b16 v[90:91], v211 offset:0x2c00
	ds_read_b64_tr_b16 v[92:93], v211 offset:0x3400
	ds_read_b64_tr_b16 v[94:95], v211 offset:0x3c00
	s_waitcnt lgkmcnt(0)
	v_mfma_f32_32x32x16_bf16 v[32:47], v[80:83], v[124:127], v[32:47]
	v_exp_f32_e32 v80, v64
	v_exp_f32_e32 v81, v65
	v_exp_f32_e32 v64, v96
	v_exp_f32_e32 v65, v97
	v_exp_f32_e32 v82, v66
	v_exp_f32_e32 v83, v67
	v_exp_f32_e32 v66, v98
	v_exp_f32_e32 v67, v99
	v_mfma_f32_32x32x16_bf16 v[32:47], v[84:87], v[120:123], v[32:47]
	v_exp_f32_e32 v84, v68
	v_exp_f32_e32 v85, v69
	v_exp_f32_e32 v68, v100
	v_exp_f32_e32 v69, v101
	v_exp_f32_e32 v86, v70
	v_exp_f32_e32 v87, v71
	v_exp_f32_e32 v70, v102
	v_exp_f32_e32 v71, v103
	v_mfma_f32_32x32x16_bf16 v[32:47], v[88:91], v[112:115], v[32:47]
	v_exp_f32_e32 v194, v72
	v_exp_f32_e32 v195, v73
	ds_read_b64_tr_b16 v[72:73], v211 offset:0x600
	v_exp_f32_e32 v196, v74
	v_exp_f32_e32 v197, v75
	ds_read_b64_tr_b16 v[74:75], v211 offset:0xe00
	v_mfma_f32_32x32x16_bf16 v[32:47], v[92:95], v[116:119], v[32:47]
	v_exp_f32_e32 v92, v76
	v_exp_f32_e32 v93, v77
	ds_read_b64_tr_b16 v[76:77], v211 offset:0x1600
	v_exp_f32_e32 v94, v78
	v_exp_f32_e32 v95, v79
	ds_read_b64_tr_b16 v[78:79], v211 offset:0x1e00
	ds_read_b64_tr_b16 v[96:97], v211 offset:0x2600
	ds_read_b64_tr_b16 v[98:99], v211 offset:0x2e00
	ds_read_b64_tr_b16 v[100:101], v211 offset:0x3600
	ds_read_b64_tr_b16 v[102:103], v211 offset:0x3e00
	s_waitcnt lgkmcnt(0)
	v_mfma_f32_32x32x16_bf16 v[16:31], v[72:75], v[124:127], v[16:31]
	v_exp_f32_e32 v72, v104
	v_exp_f32_e32 v73, v105
	v_exp_f32_e32 v74, v106
	v_exp_f32_e32 v75, v107
	v_mfma_f32_32x32x16_bf16 v[16:31], v[76:79], v[120:123], v[16:31]
	v_exp_f32_e32 v76, v108
	v_exp_f32_e32 v77, v109
	v_exp_f32_e32 v78, v110
	v_exp_f32_e32 v79, v111
	s_barrier
	v_mfma_f32_32x32x16_bf16 v[16:31], v[96:99], v[112:115], v[16:31]
	s_waitcnt vmcnt(4)
	s_waitcnt vmcnt(7)
	ds_write_b128 v212, v[178:181] offset:16384
	s_waitcnt vmcnt(6)
	ds_write_b128 v213, v[182:185] offset:16384
	s_waitcnt vmcnt(5)
	ds_write_b128 v214, v[186:189] offset:49152
	s_waitcnt vmcnt(4)
	ds_write_b128 v215, v[190:193] offset:49152
	v_mfma_f32_32x32x16_bf16 v[16:31], v[100:103], v[116:119], v[16:31]
.LBB0_885:
	v_add_f32_e32 v96, v227, v217
	s_add_i32 s2, s39, 2
	s_add_i32 s3, s39, -1
	v_add_f32_e32 v217, v229, v96
	s_cmp_ge_u32 s3, s14
	s_waitcnt lgkmcnt(0)
	s_barrier
	s_cbranch_scc1 .LBB0_887
	s_mov_b32 s39, s2
	s_branch .LBB0_881
